# baseline (speedup 1.0000x reference)
.LBB0_7:
	s_or_b64 exec, exec, s[12:13]
	s_waitcnt vmcnt(10)
	v_cmp_ne_u32_e64 s[8:9], 0, v10
	v_lshrrev_b32_e32 v0, 6, v18
	v_lshlrev_b32_e32 v0, 2, v0
	s_cmp_lg_u64 s[8:9], 0
	s_cselect_b32 s3, 1, 0
	v_mov_b32_e32 v1, s3
	ds_write_b32 v0, v1
	s_waitcnt lgkmcnt(0)
	s_barrier
	v_cmp_eq_u32_e64 s[0:1], 0, v18
	s_and_saveexec_b64 s[8:9], s[0:1]
	s_cbranch_execz .LBB0_16
	v_mov_b32_e32 v0, 0
	ds_read_b128 v[4:7], v0
	s_mov_b32 s3, 0
	s_lshl_b64 s[0:1], s[2:3], 2
	s_add_u32 s0, s28, s0
	s_addc_u32 s1, s29, s1
	v_mov_b32_e32 v0, 0x829000
	s_waitcnt lgkmcnt(0)
	v_or_b32_e32 v1, v4, v5
	v_or3_b32 v1, v1, v6, v7
	global_store_dword v0, v1, s[0:1] offset:2048 sc1

.LBB0_22:
	s_waitcnt vmcnt(8)
	v_add_f32_e32 v0, v29, v26
	s_nop 1
	v_add_f32_dpp v0, v0, v0 quad_perm:[1,0,3,2] row_mask:0xf bank_mask:0xf bound_ctrl:1
	s_nop 1
	v_add_f32_dpp v0, v0, v0 quad_perm:[2,3,0,1] row_mask:0xf bank_mask:0xf bound_ctrl:1
	s_nop 1
	v_add_f32_dpp v0, v0, v0 row_half_mirror row_mask:0xf bank_mask:0xf bound_ctrl:1
	s_nop 1
	v_add_f32_dpp v0, v0, v0 row_mirror row_mask:0xf bank_mask:0xf bound_ctrl:1
	s_nop 1
	v_readlane_b32 s44, v0, 0
	v_readlane_b32 s45, v0, 16
	v_readlane_b32 s46, v0, 32
	v_readlane_b32 s47, v0, 48
	s_mov_b32 s8, 0x7ffff8
	v_bfe_u32 v2, v14, 6, 3
	v_lshrrev_b32_e32 v3, 8, v14
	s_add_u32 s0, s28, 0x810000
	s_addc_u32 s1, s29, 0
	v_mov_b32_e32 v4, s44
	v_add_f32_e32 v4, s45, v4
	v_add_f32_e32 v4, s46, v4
	v_add_f32_e32 v4, s47, v4
	v_lshrrev_b32_e32 v0, 4, v28
	v_and_or_b32 v0, v3, s8, v0
	v_lshlrev_b32_e32 v3, 1, v27
	v_and_b32_e32 v1, 15, v18
	v_lshlrev_b32_e32 v0, 6, v0
	v_and_b32_e32 v3, 48, v3
	v_or3_b32 v0, v0, v1, v3
	v_lshl_or_b32 v0, v0, 3, v2
	v_ashrrev_i32_e32 v1, 31, v0
	v_fmac_f32_e32 v29, 0xbc000000, v4
	v_lshl_add_u64 v[2:3], v[0:1], 1, s[0:1]
	v_or_b32_e32 v0, 0x800, v0
	v_cvt_pk_bf16_f32 v5, v29, s0
	v_fmac_f32_e32 v26, 0xbc000000, v4
	v_ashrrev_i32_e32 v1, 31, v0
	global_store_short v[2:3], v5, off sc1
	v_cvt_pk_bf16_f32 v2, v26, s0
	v_lshl_add_u64 v[0:1], v[0:1], 1, s[0:1]
	global_store_short v[0:1], v2, off sc1
	s_or_b64 exec, exec, s[2:3]
	s_and_saveexec_b64 s[0:1], vcc
	s_cbranch_execz .LBB0_18
.LBB0_23:
	v_lshrrev_b32_e32 v0, 25, v15
	v_add_u32_e32 v0, v14, v0
	v_ashrrev_i32_e32 v1, 7, v0
	v_and_b32_e32 v0, 0xffffff80, v0
	v_sub_u32_e32 v0, v14, v0
	v_lshrrev_b32_e32 v5, 2, v1
	v_and_b32_e32 v3, 15, v0
	v_and_b32_e32 v5, 4, v5
	v_lshrrev_b32_e32 v0, 2, v0
	v_lshrrev_b32_e32 v4, 5, v1
	v_and_or_b32 v5, v1, 3, v5
	v_and_b32_e32 v0, 0x7ffffc, v0
	v_lshlrev_b32_e32 v1, 2, v1
	v_add_lshl_u32 v0, v0, v4, 6
	v_and_b32_e32 v1, 48, v1
	v_or3_b32 v0, v0, v3, v1
	v_lshl_or_b32 v0, v0, 3, v5
	v_ashrrev_i32_e32 v1, 31, v0
	v_lshl_add_u64 v[0:1], v[0:1], 1, s[28:29]
	v_add_co_u32_e32 v0, vcc, 0x818000, v0
	s_waitcnt vmcnt(7)
	v_cvt_pk_bf16_f32 v2, v25, s0
	v_addc_co_u32_e32 v1, vcc, 0, v1, vcc
	global_store_short v[0:1], v2, off offset:2048 sc1
	s_or_b64 exec, exec, s[0:1]
	s_and_saveexec_b64 s[0:1], s[4:5]
	s_cbranch_execz .LBB0_19
.LBB0_24:
	s_mov_b32 s2, 0x2aaaaaab
	v_mul_hi_i32 v0, v14, s2
	v_lshrrev_b32_e32 v1, 31, v0
	v_ashrrev_i32_e32 v0, 4, v0
	v_add_u32_e32 v0, v0, v1
	s_movk_i32 s2, 0x60
	v_mul_lo_u32 v1, v0, s2
	v_sub_u32_e32 v1, v14, v1
	v_lshrrev_b32_e32 v5, 2, v0
	v_and_b32_e32 v3, 15, v1
	v_and_b32_e32 v5, 4, v5
	v_lshrrev_b32_e32 v1, 2, v1
	v_lshrrev_b32_e32 v4, 5, v0
	v_and_or_b32 v5, v0, 3, v5
	v_and_b32_e32 v1, 0x7ffffc, v1
	v_lshlrev_b32_e32 v0, 2, v0
	v_add_lshl_u32 v1, v1, v4, 6
	v_and_b32_e32 v0, 48, v0
	v_or3_b32 v0, v1, v3, v0
	v_lshl_or_b32 v0, v0, 3, v5
	v_ashrrev_i32_e32 v1, 31, v0
	v_lshl_add_u64 v[0:1], v[0:1], 1, s[28:29]
	v_add_co_u32_e32 v0, vcc, 0x820000, v0
	s_waitcnt vmcnt(6)
	v_cvt_pk_bf16_f32 v2, v24, s0
	v_addc_co_u32_e32 v1, vcc, 0, v1, vcc
	global_store_short v[0:1], v2, off offset:2048 sc1
	s_or_b64 exec, exec, s[0:1]
	s_and_saveexec_b64 s[0:1], s[6:7]
	s_cbranch_execz .LBB0_20
.LBB0_25:
	v_lshrrev_b32_e32 v0, 26, v15
	v_add_u32_e32 v0, v14, v0
	v_ashrrev_i32_e32 v1, 6, v0
	v_and_b32_e32 v0, 0xffffffc0, v0
	v_sub_u32_e32 v0, v14, v0
	v_lshrrev_b32_e32 v5, 2, v1
	v_lshrrev_b32_e32 v3, 4, v0
	v_and_b32_e32 v5, 4, v5
	v_lshrrev_b32_e32 v4, 5, v1
	v_and_or_b32 v5, v1, 3, v5
	v_lshl_add_u32 v3, v3, 1, v3
	v_lshlrev_b32_e32 v1, 2, v1
	v_and_b32_e32 v0, 15, v0
	v_add_lshl_u32 v3, v3, v4, 6
	v_and_b32_e32 v1, 48, v1
	v_or3_b32 v0, v3, v0, v1
	v_lshl_or_b32 v0, v0, 3, v5
	v_ashrrev_i32_e32 v1, 31, v0
	v_lshl_add_u64 v[0:1], v[0:1], 1, s[28:29]
	v_add_co_u32_e32 v0, vcc, 0x826000, v0
	s_waitcnt vmcnt(5)
	v_cvt_pk_bf16_f32 v2, v23, s0
	v_addc_co_u32_e32 v1, vcc, 0, v1, vcc
	global_store_short v[0:1], v2, off offset:2048 sc1
	s_or_b64 exec, exec, s[0:1]
	s_and_saveexec_b64 s[0:1], s[10:11]
	s_cbranch_execz .LBB0_21
.LBB0_26:
	s_waitcnt vmcnt(0)
	v_add_f32_e32 v0, v30, v31
	s_nop 1
	v_add_f32_dpp v0, v0, v0 quad_perm:[1,0,3,2] row_mask:0xf bank_mask:0xf bound_ctrl:1
	s_nop 1
	v_add_f32_dpp v0, v0, v0 quad_perm:[2,3,0,1] row_mask:0xf bank_mask:0xf bound_ctrl:1
	s_nop 1
	v_add_f32_dpp v0, v0, v0 row_half_mirror row_mask:0xf bank_mask:0xf bound_ctrl:1
	s_nop 1
	v_add_f32_dpp v0, v0, v0 row_mirror row_mask:0xf bank_mask:0xf bound_ctrl:1
	s_nop 1
	v_readlane_b32 s44, v0, 0
	v_readlane_b32 s45, v0, 16
	v_readlane_b32 s46, v0, 32
	v_readlane_b32 s47, v0, 48
	v_mov_b32_e32 v17, s44
	v_add_f32_e32 v17, s45, v17
	v_add_f32_e32 v17, s46, v17
	v_add_f32_e32 v17, s47, v17
	v_lshl_add_u64 v[0:1], v[14:15], 2, s[28:29]
	s_mov_b64 s[0:1], 0x818000
	v_lshl_add_u64 v[2:3], v[0:1], 0, s[0:1]
	v_add_co_u32_e32 v0, vcc, 0x818000, v0
	v_fmamk_f32 v6, v17, 0xbc000000, v16
	v_addc_co_u32_e32 v1, vcc, 0, v1, vcc
	v_mul_f32_e32 v4, 0x4038aa3b, v22
	v_mul_f32_e32 v5, 0x4038aa3b, v19
	global_store_dword v[0:1], v6, off sc1
	global_store_dword v[2:3], v5, off offset:512 sc1
	global_store_dword v[2:3], v4, off offset:1024 sc1
	s_endpgm
